# down-projection phase walks its units in reverse order: it starts on the activation rows the gate/up phase wrote last (still in the last-level cache)
# speedup vs baseline: 1.0096x; 1.0081x over previous
; #define LAS __attribute__((address_space(3)))
; DI int my_tid() { return wave_in_wg() * 64 + lane_id(); }
; DI void moe_tables(const Params& P, LAS unsigned char* lds, int npn, int G, int bid) {
;     LAS int* tab = (LAS int*)(lds + LDS_CTL_OFF + 64); LAS int* ul = (LAS int*)(lds + LDS_CTL_OFF + 384);
;     __syncthreads();
;     if (my_tid() == 0) { const unsigned* gc = (const unsigned*)(P.ws + WS_CTL) + CW_GCNT; int pre = 0;
;         for (int e = 0; e < NE; ++e) { const int cn = (int)__hip_atomic_load(gc + e, __ATOMIC_RELAXED, __HIP_MEMORY_SCOPE_AGENT); tab[e] = cn; tab[32 + e] = pre; pre += (cn + 255) >> 8; }
;         tab[64] = pre; }
;     __syncthreads();
;     if (npn > 0 && my_tid() < 64) { const int i = my_tid(); const int nwg = tab[64] * npn; const int L = i * G + bid; int d0 = -1, d1 = 0;
.LBB0_1315:
	s_or_b64 exec, exec, s[4:5]
	s_waitcnt lgkmcnt(0)
	s_barrier
	s_getreg_b32 s2, hwreg(HW_REG_HW_ID, 0, 6)
	s_and_b32 s2, s2, 63
	s_lshl_b32 s2, s2, 2
	s_add_i32 s2, s2, 0
	s_add_i32 s2, s2, 0x24400
	v_mov_b32_e32 v0, s2
	ds_read_b32 v0, v0
	s_waitcnt lgkmcnt(0)
	v_readfirstlane_b32 s2, v0
	v_mbcnt_lo_u32_b32 v0, -1, 0
	v_mbcnt_hi_u32_b32 v0, -1, v0
	s_nop 1
	v_lshl_add_u32 v0, s2, 6, v0
	v_cmp_gt_i32_e32 vcc, 64, v0
	s_and_saveexec_b64 s[4:5], vcc
	s_cbranch_execz .LBB0_1319
	s_getreg_b32 s2, hwreg(HW_REG_HW_ID, 0, 6)
	s_and_b32 s2, s2, 63
	s_lshl_b32 s2, s2, 2
	s_add_i32 s2, s2, 0
	s_add_i32 s2, s2, 0x24400
	v_mov_b32_e32 v0, s2
	ds_read_b32 v0, v0
	s_add_i32 s2, 0, 0x24140
	v_mov_b32_e32 v2, s2
	v_mbcnt_lo_u32_b32 v1, -1, 0
	v_mbcnt_hi_u32_b32 v1, -1, v1
	ds_read_b32 v3, v2
	s_waitcnt lgkmcnt(1)
	v_readfirstlane_b32 s2, v0
	s_waitcnt lgkmcnt(0)
	v_lshlrev_b32_e32 v0, 3, v3
	v_lshl_add_u32 v2, s2, 6, v1
	v_readlane_b32 s2, v254, 18
	v_readlane_b32 s3, v254, 19
	s_nop 0
	v_mul_lo_u32 v1, v2, s2
	v_readlane_b32 s2, v254, 0
	v_readlane_b32 s3, v254, 1
	s_nop 0
	v_add_u32_e32 v4, s2, v1
	v_cmp_lt_i32_e32 vcc, v4, v0
	v_mov_b32_e32 v1, 0
	v_mov_b32_e32 v0, -1
	s_and_saveexec_b64 s[6:7], vcc
	s_cbranch_execz .LBB0_1318
; DI int my_tid() { return wave_in_wg() * 64 + lane_id(); }
; __device__ __forceinline__ int xcd_remap(int L, int nwg) { const int q = nwg / NXCD, r = nwg % NXCD, xcd = L % NXCD, off = L / NXCD; return (xcd < r ? xcd * (q + 1) : r * (q + 1) + (xcd - r) * q) + off; }
; DI void moe_tables(const Params& P, LAS unsigned char* lds, int npn, int G, int bid) {
;     ...
;     if (npn > 0 && my_tid() < 64) { const int i = my_tid(); const int nwg = tab[64] * npn; const int L = i * G + bid; int d0 = -1, d1 = 0;
;         if (L < nwg) { const int wg = pg8::xcd_remap(L, nwg); int e = 0;
;             for (int k = 1; k < 32; ++k) if (wg >= tab[32 + k] * npn) e = k;
;             const int t0 = tab[32 + e], nM = tab[32 + e + 1] - t0, w = wg - t0 * npn; int pm, pn; pg8::tile_order(w, nM * npn, nM, npn, pm, pn);
;             d0 = e | (pn << 8) | (pm << 16); d1 = t0; }
;         ul[2 * i] = d0; ul[2 * i + 1] = d1; }
	v_ashrrev_i32_e32 v0, 31, v4
	v_lshrrev_b32_e32 v0, 29, v0
	v_add_u32_e32 v1, v4, v0
	v_ashrrev_i32_e32 v0, 3, v1
	v_and_b32_e32 v1, -8, v1
	v_sub_u32_e32 v1, v4, v1
	v_lshrrev_b32_e32 v4, 31, v1
	v_add_u32_e32 v3, v3, v4
	v_mad_u64_u32 v[0:1], s[2:3], v1, v3, v[0:1]
	v_mov_b32_e32 v30, 0x24140
	ds_read_b32 v30, v30
	s_waitcnt lgkmcnt(0)
	v_lshlrev_b32_e32 v30, 3, v30
	v_add_u32_e32 v30, -1, v30
	v_sub_u32_e32 v0, v30, v0
	s_add_i32 s2, 0, 0x240c4
	s_nop 0
	v_mov_b32_e32 v1, s2
	ds_read2_b32 v[4:5], v1 offset1:1
	s_add_i32 s2, 0, 0x240cc
	v_mov_b32_e32 v1, s2
	s_add_i32 s2, 0, 0x240d4
	v_mov_b32_e32 v3, s2
	s_add_i32 s2, 0, 0x240dc
	v_mov_b32_e32 v10, s2
	ds_read2_b32 v[6:7], v1 offset1:1
	ds_read2_b32 v[8:9], v3 offset1:1
	ds_read2_b32 v[10:11], v10 offset1:1
	s_waitcnt lgkmcnt(3)
	v_lshlrev_b32_e32 v1, 3, v4
	v_cmp_ge_i32_e32 vcc, v0, v1
	v_lshlrev_b32_e32 v3, 3, v5
	s_add_i32 s2, 0, 0x240e4
	v_cndmask_b32_e64 v1, 0, 1, vcc
	v_cmp_lt_i32_e32 vcc, v0, v3
	s_waitcnt lgkmcnt(2)
	v_lshlrev_b32_e32 v3, 3, v6
	v_cndmask_b32_e32 v1, 2, v1, vcc
	v_cmp_lt_i32_e32 vcc, v0, v3
	v_lshlrev_b32_e32 v3, 3, v7
	s_nop 0
	v_cndmask_b32_e32 v1, 3, v1, vcc
	v_cmp_lt_i32_e32 vcc, v0, v3
	s_waitcnt lgkmcnt(1)
	v_lshlrev_b32_e32 v3, 3, v8
	v_cndmask_b32_e32 v1, 4, v1, vcc
	v_cmp_lt_i32_e32 vcc, v0, v3
	v_lshlrev_b32_e32 v3, 3, v9
	s_nop 0
	v_cndmask_b32_e32 v1, 5, v1, vcc
	v_cmp_lt_i32_e32 vcc, v0, v3
	s_waitcnt lgkmcnt(0)
	v_lshlrev_b32_e32 v3, 3, v10
	v_cndmask_b32_e32 v1, 6, v1, vcc
	v_cmp_lt_i32_e32 vcc, v0, v3
	v_lshlrev_b32_e32 v3, 3, v11
	s_nop 0
	v_cndmask_b32_e32 v1, 7, v1, vcc
	v_cmp_lt_i32_e32 vcc, v0, v3
	v_mov_b32_e32 v3, s2
	ds_read2_b32 v[4:5], v3 offset1:1
	s_add_i32 s2, 0, 0x240ec
	v_mov_b32_e32 v3, s2
	s_add_i32 s2, 0, 0x240f4
	v_mov_b32_e32 v8, s2
	s_add_i32 s2, 0, 0x240fc
	v_mov_b32_e32 v10, s2
	ds_read2_b32 v[6:7], v3 offset1:1
	ds_read2_b32 v[8:9], v8 offset1:1
	ds_read2_b32 v[10:11], v10 offset1:1
	s_waitcnt lgkmcnt(3)
	v_lshlrev_b32_e32 v3, 3, v4
	v_cndmask_b32_e32 v1, 8, v1, vcc
	v_cmp_lt_i32_e32 vcc, v0, v3
	v_lshlrev_b32_e32 v3, 3, v5
	s_add_i32 s2, 0, 0x24104
	v_cndmask_b32_e32 v1, 9, v1, vcc
	v_cmp_lt_i32_e32 vcc, v0, v3
	s_waitcnt lgkmcnt(2)
	v_lshlrev_b32_e32 v3, 3, v6
	v_cndmask_b32_e32 v1, 10, v1, vcc
	v_cmp_lt_i32_e32 vcc, v0, v3
	v_lshlrev_b32_e32 v3, 3, v7
	s_nop 0
	v_cndmask_b32_e32 v1, 11, v1, vcc
	v_cmp_lt_i32_e32 vcc, v0, v3
	s_waitcnt lgkmcnt(1)
	v_lshlrev_b32_e32 v3, 3, v8
	v_cndmask_b32_e32 v1, 12, v1, vcc
	v_cmp_lt_i32_e32 vcc, v0, v3
	v_lshlrev_b32_e32 v3, 3, v9
	s_nop 0
	v_cndmask_b32_e32 v1, 13, v1, vcc
	v_cmp_lt_i32_e32 vcc, v0, v3
	s_waitcnt lgkmcnt(0)
	v_lshlrev_b32_e32 v3, 3, v10
	v_cndmask_b32_e32 v1, 14, v1, vcc
	v_cmp_lt_i32_e32 vcc, v0, v3
	v_lshlrev_b32_e32 v3, 3, v11
	s_nop 0
	v_cndmask_b32_e32 v1, 15, v1, vcc
	v_cmp_lt_i32_e32 vcc, v0, v3
	v_mov_b32_e32 v3, s2
	ds_read2_b32 v[4:5], v3 offset1:1
	s_add_i32 s2, 0, 0x2410c
	v_mov_b32_e32 v3, s2
	s_add_i32 s2, 0, 0x24114
	v_mov_b32_e32 v8, s2
	s_add_i32 s2, 0, 0x2411c
	v_mov_b32_e32 v10, s2
	ds_read2_b32 v[6:7], v3 offset1:1
	ds_read2_b32 v[8:9], v8 offset1:1
	ds_read2_b32 v[10:11], v10 offset1:1
	s_waitcnt lgkmcnt(3)
	v_lshlrev_b32_e32 v3, 3, v4
	v_cndmask_b32_e32 v1, 16, v1, vcc
	v_cmp_lt_i32_e32 vcc, v0, v3
	v_lshlrev_b32_e32 v3, 3, v5
	s_add_i32 s2, 0, 0x24124
	v_cndmask_b32_e32 v1, 17, v1, vcc
	v_cmp_lt_i32_e32 vcc, v0, v3
	s_waitcnt lgkmcnt(2)
	v_lshlrev_b32_e32 v3, 3, v6
	v_cndmask_b32_e32 v1, 18, v1, vcc
	v_cmp_lt_i32_e32 vcc, v0, v3
	v_lshlrev_b32_e32 v3, 3, v7
	s_nop 0
	v_cndmask_b32_e32 v1, 19, v1, vcc
	v_cmp_lt_i32_e32 vcc, v0, v3
	s_waitcnt lgkmcnt(1)
	v_lshlrev_b32_e32 v3, 3, v8
	v_cndmask_b32_e32 v1, 20, v1, vcc
	v_cmp_lt_i32_e32 vcc, v0, v3
	v_lshlrev_b32_e32 v3, 3, v9
	s_nop 0
	v_cndmask_b32_e32 v1, 21, v1, vcc
	v_cmp_lt_i32_e32 vcc, v0, v3
	s_waitcnt lgkmcnt(0)
	v_lshlrev_b32_e32 v3, 3, v10
	v_cndmask_b32_e32 v1, 22, v1, vcc
	v_cmp_lt_i32_e32 vcc, v0, v3
	v_lshlrev_b32_e32 v3, 3, v11
	s_nop 0
	v_cndmask_b32_e32 v1, 23, v1, vcc
	v_cmp_lt_i32_e32 vcc, v0, v3
	v_mov_b32_e32 v3, s2
	ds_read2_b32 v[4:5], v3 offset1:1
	s_add_i32 s2, 0, 0x2412c
	v_mov_b32_e32 v3, s2
	s_add_i32 s2, 0, 0x24134
	v_mov_b32_e32 v8, s2
	s_add_i32 s2, 0, 0x2413c
	v_mov_b32_e32 v10, s2
	ds_read2_b32 v[6:7], v3 offset1:1
	ds_read2_b32 v[8:9], v8 offset1:1
	ds_read_b32 v3, v10
	s_waitcnt lgkmcnt(3)
	v_lshlrev_b32_e32 v4, 3, v4
	v_cndmask_b32_e32 v1, 24, v1, vcc
	v_cmp_lt_i32_e32 vcc, v0, v4
	v_lshlrev_b32_e32 v4, 3, v5
	s_waitcnt lgkmcnt(0)
	v_lshlrev_b32_e32 v3, 3, v3
	v_cndmask_b32_e32 v1, 25, v1, vcc
	v_cmp_lt_i32_e32 vcc, v0, v4
	v_lshlrev_b32_e32 v4, 3, v6
	s_add_i32 s2, 0, 0x24040
	v_cndmask_b32_e32 v1, 26, v1, vcc
	v_cmp_lt_i32_e32 vcc, v0, v4
	v_lshlrev_b32_e32 v4, 3, v7
	s_nop 0
	v_cndmask_b32_e32 v1, 27, v1, vcc
	v_cmp_lt_i32_e32 vcc, v0, v4
	v_lshlrev_b32_e32 v4, 3, v8
	s_nop 0
	v_cndmask_b32_e32 v1, 28, v1, vcc
	v_cmp_lt_i32_e32 vcc, v0, v4
	v_lshlrev_b32_e32 v4, 3, v9
	s_nop 0
	v_cndmask_b32_e32 v1, 29, v1, vcc
	v_cmp_lt_i32_e32 vcc, v0, v4
	s_nop 1
	v_cndmask_b32_e32 v1, 30, v1, vcc
	v_cmp_lt_i32_e32 vcc, v0, v3
	s_nop 1
	v_cndmask_b32_e32 v1, 31, v1, vcc
	v_lshl_add_u32 v3, v1, 2, s2
	ds_read2_b32 v[4:5], v3 offset0:32 offset1:33
	s_waitcnt lgkmcnt(0)
	v_lshlrev_b32_e32 v3, 3, v4
	v_sub_u32_e32 v0, v0, v3
	v_ashrrev_i32_e32 v3, 31, v0
	v_lshrrev_b32_e32 v3, 26, v3
	v_add_u32_e32 v3, v0, v3
	v_ashrrev_i32_e32 v6, 6, v3
	v_lshlrev_b32_e32 v6, 3, v6
	v_add_u32_e32 v7, v4, v6
	v_sub_u32_e32 v5, v5, v7
	v_min_i32_e32 v5, 8, v5
	v_sub_u32_e32 v7, 0, v5
	v_max_i32_e32 v7, v5, v7
	v_cvt_f32_u32_e32 v8, v7
	v_and_b32_e32 v3, 0xffffffc0, v3
	v_sub_u32_e32 v10, 0, v7
	v_sub_u32_e32 v0, v0, v3
	v_rcp_iflag_f32_e32 v8, v8
	v_sub_u32_e32 v9, 0, v0
	v_max_i32_e32 v9, v0, v9
	v_xor_b32_e32 v3, v0, v5
	v_mul_f32_e32 v8, 0x4f7ffffe, v8
	v_cvt_u32_f32_e32 v8, v8
	v_ashrrev_i32_e32 v3, 31, v3
	v_mul_lo_u32 v10, v10, v8
	v_mul_hi_u32 v10, v8, v10
	v_add_u32_e32 v8, v8, v10
	v_mul_hi_u32 v8, v9, v8
	v_mul_lo_u32 v10, v8, v7
	v_sub_u32_e32 v9, v9, v10
	v_add_u32_e32 v10, 1, v8
	v_cmp_ge_u32_e32 vcc, v9, v7
	s_nop 1
	v_cndmask_b32_e32 v8, v8, v10, vcc
	v_sub_u32_e32 v10, v9, v7
	v_cndmask_b32_e32 v9, v9, v10, vcc
	v_add_u32_e32 v10, 1, v8
	v_cmp_ge_u32_e32 vcc, v9, v7
	s_nop 1
	v_cndmask_b32_e32 v7, v8, v10, vcc
	v_xor_b32_e32 v7, v7, v3
	v_sub_u32_e32 v3, v7, v3
	v_mul_lo_u32 v5, v3, v5
	v_sub_u32_e32 v0, v0, v5
	v_lshlrev_b32_e32 v3, 8, v3
	v_add_lshl_u32 v0, v6, v0, 16
	v_or3_b32 v0, v3, v0, v1
	v_mov_b32_e32 v1, v4
